# MoE GEMM 1 unit header: duplicate expert-id LDS read removed, on the mixer-heavy schedule stack
# speedup vs baseline: 1.0118x; 1.0118x over previous
.LBB0_1785:
	s_add_i32 s53, s63, 1
	s_mul_i32 s16, s53, s3
	s_add_i32 s21, s16, s87
	s_ashr_i32 s54, s21, 3
	s_cmp_lt_i32 s54, s26
	s_cselect_b64 s[16:17], -1, 0
	s_and_b32 s61, s21, 7
	s_cmp_ge_i32 s54, s26
	s_mov_b32 s58, s20
	s_cbranch_scc1 .LBB0_1787
	s_add_i32 s14, s54, 0
	s_add_i32 s14, s14, 0x20400
	v_mov_b32_e32 v4, s14
	v_mbcnt_lo_u32_b32 v0, -1, 0
	v_mbcnt_hi_u32_b32 v0, -1, v0
	ds_read_u8 v2, v4
	s_add_i32 s14, s58, 0
	s_add_i32 m0, s14, 0x25000
	v_lshlrev_b32_e32 v3, 5, v0
	v_lshlrev_b32_e32 v0, 4, v0
	s_waitcnt lgkmcnt(0)
	v_readfirstlane_b32 s14, v2
	s_mov_b32 s20, s14
	s_lshl_b32 s14, s14, 11
	s_ashr_i32 s15, s14, 31
	s_lshl_b64 s[14:15], s[14:15], 2
	s_add_u32 s14, s29, s14
	v_and_b32_e32 v2, 0xfffffc00, v3
	s_addc_u32 s15, s30, s15
	v_ashrrev_i32_e32 v3, 31, v2
	v_lshl_add_u64 v[2:3], v[2:3], 2, s[14:15]
	s_lshl_b32 s70, s61, 9
	v_lshl_add_u64 v[2:3], v[2:3], 0, s[70:71]
	v_and_b32_e32 v0, 0x1f0, v0
	v_lshl_add_u64 v[2:3], v[2:3], 0, v[0:1]
	global_load_lds_dwordx4 v[2:3], off
	s_mov_b32 s14, s20
	s_ashr_i32 s15, s14, 31
	s_lshl_b64 s[14:15], s[14:15], 21
	s_add_u32 s14, s27, s14
	s_addc_u32 s15, s28, s15
	s_lshl_b32 s20, s61, 18
	s_add_u32 s14, s14, s20
	s_addc_u32 s15, s15, 0
